# MLA: merged QK waits per k-step, simplified l bookkeeping in fast path, causal mask via e64 compares with inline constants (2 instr/elem)
# speedup vs baseline: 1.0237x; 1.0084x over previous
.LBB0_1242:
	s_and_b32 s14, s14, 2
	s_mulk_i32 s14, 0x6000
	s_waitcnt lgkmcnt(6)
	v_mfma_f32_32x32x16_bf16 v[80:95], v[64:67], v[112:115], 0
	v_mfma_f32_32x32x16_bf16 v[64:79], v[68:71], v[112:115], 0
	s_waitcnt lgkmcnt(4)
	v_mfma_f32_32x32x16_bf16 v[80:95], v[160:163], v[116:119], v[80:95]
	ds_read_b128 v[160:163], v144 offset:128
	ds_read_b128 v[216:219], v144 offset:12416
	v_mfma_f32_32x32x16_bf16 v[64:79], v[164:167], v[116:119], v[64:79]
	s_waitcnt lgkmcnt(4)
	v_mfma_f32_32x32x16_bf16 v[80:95], v[176:179], v[120:123], v[80:95]
	ds_read_b128 v[164:167], v146 offset:128
	ds_read_b128 v[176:179], v146 offset:12416
	v_mfma_f32_32x32x16_bf16 v[64:79], v[204:207], v[120:123], v[64:79]
	s_waitcnt lgkmcnt(4)
	v_mfma_f32_32x32x16_bf16 v[80:95], v[208:211], v[124:127], v[80:95]
	ds_read_b128 v[204:207], v159 offset:128
	ds_read_b128 v[208:211], v159 offset:12416
	v_mfma_f32_32x32x16_bf16 v[64:79], v[212:215], v[124:127], v[64:79]
	s_waitcnt lgkmcnt(4)
	v_mfma_f32_32x32x16_bf16 v[80:95], v[160:163], v[96:99], v[80:95]
	ds_read_b128 v[160:163], v168 offset:128
	ds_read_b128 v[212:215], v168 offset:12416
	v_mfma_f32_32x32x16_bf16 v[64:79], v[216:219], v[96:99], v[64:79]
	s_waitcnt lgkmcnt(4)
	v_mfma_f32_32x32x16_bf16 v[80:95], v[164:167], v[100:103], v[80:95]
	ds_read_b128 v[164:167], v144 offset:256
	ds_read_b128 v[216:219], v144 offset:12544
	v_mfma_f32_32x32x16_bf16 v[64:79], v[176:179], v[100:103], v[64:79]
	s_waitcnt lgkmcnt(4)
	v_mfma_f32_32x32x16_bf16 v[80:95], v[204:207], v[104:107], v[80:95]
	ds_read_b128 v[176:179], v146 offset:256
	ds_read_b128 v[204:207], v146 offset:12544
	v_mfma_f32_32x32x16_bf16 v[64:79], v[208:211], v[104:107], v[64:79]
	s_waitcnt lgkmcnt(4)
	v_mfma_f32_32x32x16_bf16 v[80:95], v[160:163], v[108:111], v[80:95]
	ds_read_b128 v[160:163], v159 offset:256
	ds_read_b128 v[208:211], v159 offset:12544
	v_mfma_f32_32x32x16_bf16 v[64:79], v[212:215], v[108:111], v[64:79]
	s_waitcnt lgkmcnt(4)
	v_mfma_f32_32x32x16_bf16 v[80:95], v[164:167], v[128:131], v[80:95]
	ds_read_b128 v[164:167], v168 offset:256
	ds_read_b128 v[212:215], v168 offset:12544
	v_mfma_f32_32x32x16_bf16 v[64:79], v[216:219], v[128:131], v[64:79]
	s_waitcnt lgkmcnt(4)
	v_mfma_f32_32x32x16_bf16 v[80:95], v[176:179], v[132:135], v[80:95]
	v_mfma_f32_32x32x16_bf16 v[64:79], v[204:207], v[132:135], v[64:79]
	s_waitcnt lgkmcnt(2)
	v_mfma_f32_32x32x16_bf16 v[80:95], v[160:163], v[136:139], v[80:95]
	v_mfma_f32_32x32x16_bf16 v[64:79], v[208:211], v[136:139], v[64:79]
	s_waitcnt lgkmcnt(0)
	v_mfma_f32_32x32x16_bf16 v[80:95], v[164:167], v[140:143], v[80:95]
	v_mfma_f32_32x32x16_bf16 v[64:79], v[212:215], v[140:143], v[64:79]
	s_sub_i32 s15, s7, 64
	s_cmp_le_u32 s15, s44
	s_cbranch_scc1 .LBB0_1244
	v_add_u32_e32 v144, 123, v156
	v_cmp_le_i32_e64 s[16:17], 0, v144
	v_cmp_le_i32_e64 s[18:19], 32, v144
	v_cmp_le_i32_e64 vcc, 1, v144
	s_nop 4
	v_cndmask_b32_e64 v80, v199, v80, s[16:17]
	v_cmp_le_i32_e64 s[16:17], 33, v144
	v_cndmask_b32_e64 v64, v199, v64, s[18:19]
	v_cmp_le_i32_e64 s[18:19], 2, v144
	v_cndmask_b32_e64 v81, v199, v81, vcc
	v_cmp_le_i32_e64 vcc, 34, v144
	v_cndmask_b32_e64 v65, v199, v65, s[16:17]
	v_cmp_le_i32_e64 s[16:17], 3, v144
	v_cndmask_b32_e64 v82, v199, v82, s[18:19]
	v_cmp_le_i32_e64 s[18:19], 35, v144
	v_cndmask_b32_e64 v66, v199, v66, vcc
	v_cmp_le_i32_e64 vcc, 8, v144
	v_cndmask_b32_e64 v83, v199, v83, s[16:17]
	v_cmp_le_i32_e64 s[16:17], 40, v144
	v_cndmask_b32_e64 v67, v199, v67, s[18:19]
	v_cmp_le_i32_e64 s[18:19], 9, v144
	v_cndmask_b32_e64 v84, v199, v84, vcc
	v_cmp_le_i32_e64 vcc, 41, v144
	v_cndmask_b32_e64 v68, v199, v68, s[16:17]
	v_cmp_le_i32_e64 s[16:17], 10, v144
	v_cndmask_b32_e64 v85, v199, v85, s[18:19]
	v_cmp_le_i32_e64 s[18:19], 42, v144
	v_cndmask_b32_e64 v69, v199, v69, vcc
	v_cmp_le_i32_e64 vcc, 11, v144
	v_cndmask_b32_e64 v86, v199, v86, s[16:17]
	v_cmp_le_i32_e64 s[16:17], 43, v144
	v_cndmask_b32_e64 v70, v199, v70, s[18:19]
	v_cmp_le_i32_e64 s[18:19], 16, v144
	v_cndmask_b32_e64 v87, v199, v87, vcc
	v_cmp_le_i32_e64 vcc, 48, v144
	v_cndmask_b32_e64 v71, v199, v71, s[16:17]
	v_cmp_le_i32_e64 s[16:17], 17, v144
	v_cndmask_b32_e64 v88, v199, v88, s[18:19]
	v_cmp_le_i32_e64 s[18:19], 49, v144
	v_cndmask_b32_e64 v72, v199, v72, vcc
	v_cmp_le_i32_e64 vcc, 18, v144
	v_cndmask_b32_e64 v89, v199, v89, s[16:17]
	v_cmp_le_i32_e64 s[16:17], 50, v144
	v_cndmask_b32_e64 v73, v199, v73, s[18:19]
	v_cmp_le_i32_e64 s[18:19], 19, v144
	v_cndmask_b32_e64 v90, v199, v90, vcc
	v_cmp_le_i32_e64 vcc, 51, v144
	v_cndmask_b32_e64 v74, v199, v74, s[16:17]
	v_cmp_le_i32_e64 s[16:17], 24, v144
	v_cndmask_b32_e64 v91, v199, v91, s[18:19]
	v_cmp_le_i32_e64 s[18:19], 56, v144
	v_cndmask_b32_e64 v75, v199, v75, vcc
	v_cmp_le_i32_e64 vcc, 25, v144
	v_cndmask_b32_e64 v92, v199, v92, s[16:17]
	v_cmp_le_i32_e64 s[16:17], 57, v144
	v_cndmask_b32_e64 v76, v199, v76, s[18:19]
	v_cmp_le_i32_e64 s[18:19], 26, v144
	v_cndmask_b32_e64 v93, v199, v93, vcc
	v_cmp_le_i32_e64 vcc, 58, v144
	v_cndmask_b32_e64 v77, v199, v77, s[16:17]
	v_cmp_le_i32_e64 s[16:17], 27, v144
	v_cndmask_b32_e64 v94, v199, v94, s[18:19]
	v_cmp_le_i32_e64 s[18:19], 59, v144
	v_cndmask_b32_e64 v78, v199, v78, vcc
	v_cndmask_b32_e64 v95, v199, v95, s[16:17]
	v_cndmask_b32_e64 v79, v199, v79, s[18:19]

.LBB0_1246:
	v_sub_f32_e32 v80, v80, v157
	v_exp_f32_e32 v80, v80
	v_sub_f32_e32 v81, v81, v157
	v_exp_f32_e32 v81, v81
	v_sub_f32_e32 v82, v82, v157
	v_exp_f32_e32 v82, v82
	v_sub_f32_e32 v83, v83, v157
	v_exp_f32_e32 v83, v83
	v_sub_f32_e32 v84, v84, v157
	v_add_f32_e32 v146, 0, v80
	v_exp_f32_e32 v84, v84
	v_sub_f32_e32 v85, v85, v157
	v_add_f32_e32 v146, v81, v146
	v_exp_f32_e32 v85, v85
	v_sub_f32_e32 v86, v86, v157
	v_add_f32_e32 v146, v82, v146
	v_exp_f32_e32 v86, v86
	v_sub_f32_e32 v87, v87, v157
	v_add_f32_e32 v146, v83, v146
	v_exp_f32_e32 v87, v87
	v_sub_f32_e32 v88, v88, v157
	v_add_f32_e32 v146, v84, v146
	v_exp_f32_e32 v88, v88
	v_sub_f32_e32 v89, v89, v157
	v_add_f32_e32 v146, v85, v146
	v_exp_f32_e32 v89, v89
	v_sub_f32_e32 v90, v90, v157
	v_add_f32_e32 v146, v86, v146
	v_exp_f32_e32 v90, v90
	v_sub_f32_e32 v91, v91, v157
	v_add_f32_e32 v146, v87, v146
	v_exp_f32_e32 v91, v91
	v_sub_f32_e32 v92, v92, v157
	v_add_f32_e32 v146, v88, v146
	v_exp_f32_e32 v92, v92
	v_sub_f32_e32 v93, v93, v157
	v_add_f32_e32 v146, v89, v146
	v_exp_f32_e32 v93, v93
	v_sub_f32_e32 v94, v94, v157
	v_add_f32_e32 v146, v90, v146
	v_exp_f32_e32 v94, v94
	v_sub_f32_e32 v95, v95, v157
	v_add_f32_e32 v146, v91, v146
	v_exp_f32_e32 v95, v95
	v_sub_f32_e32 v64, v64, v157
	v_add_f32_e32 v146, v92, v146
	v_exp_f32_e32 v64, v64
	v_sub_f32_e32 v65, v65, v157
	v_add_f32_e32 v146, v93, v146
	v_exp_f32_e32 v65, v65
	v_sub_f32_e32 v66, v66, v157
	v_add_f32_e32 v146, v94, v146
	v_exp_f32_e32 v66, v66
	v_sub_f32_e32 v67, v67, v157
	v_add_f32_e32 v146, v95, v146
	v_exp_f32_e32 v67, v67
	v_sub_f32_e32 v68, v68, v157
	v_add_f32_e32 v146, v64, v146
	v_exp_f32_e32 v68, v68
	v_sub_f32_e32 v69, v69, v157
	v_add_f32_e32 v146, v65, v146
	v_exp_f32_e32 v69, v69
	v_sub_f32_e32 v70, v70, v157
	v_add_f32_e32 v146, v66, v146
	v_exp_f32_e32 v70, v70
	v_sub_f32_e32 v71, v71, v157
	v_add_f32_e32 v146, v67, v146
	v_exp_f32_e32 v71, v71
	v_sub_f32_e32 v72, v72, v157
	v_add_f32_e32 v146, v68, v146
	v_exp_f32_e32 v161, v72
	v_add_f32_e32 v146, v69, v146
	v_add_f32_e32 v146, v70, v146
	v_add_f32_e32 v146, v71, v146
	v_sub_f32_e32 v73, v73, v157
	v_add_f32_e32 v72, v161, v146
	v_exp_f32_e32 v146, v73
	v_sub_f32_e32 v73, v74, v157
	v_exp_f32_e32 v162, v73
	v_sub_f32_e32 v73, v75, v157
	v_exp_f32_e32 v163, v73
	v_sub_f32_e32 v73, v76, v157
	v_exp_f32_e32 v164, v73
	v_sub_f32_e32 v73, v77, v157
	v_add_f32_e32 v72, v146, v72
	v_exp_f32_e32 v165, v73
	v_sub_f32_e32 v73, v78, v157
	v_add_f32_e32 v72, v162, v72
	v_exp_f32_e32 v166, v73
	v_sub_f32_e32 v73, v79, v157
	v_add_f32_e32 v72, v163, v72
	v_exp_f32_e32 v167, v73
	v_add_f32_e32 v72, v164, v72
	v_add_f32_e32 v72, v165, v72
	v_add_f32_e32 v72, v166, v72
	v_cvt_pk_bf16_f32 v76, v80, v81
	v_cvt_pk_bf16_f32 v77, v84, v85
	v_cvt_pk_bf16_f32 v78, v82, v83
	v_cvt_pk_bf16_f32 v79, v86, v87
	v_cvt_pk_bf16_f32 v64, v64, v65
	v_cvt_pk_bf16_f32 v65, v68, v69
	v_cvt_pk_bf16_f32 v68, v161, v146
	v_add_u32_e32 v146, s14, v151
	v_add_f32_e32 v159, v167, v72
	v_cvt_pk_bf16_f32 v72, v88, v89
	v_cvt_pk_bf16_f32 v73, v92, v93
	v_cvt_pk_bf16_f32 v74, v90, v91
	v_cvt_pk_bf16_f32 v75, v94, v95
	v_add_u32_e32 v161, s14, v152
	ds_read_b64_tr_b16 v[80:81], v146
	ds_read_b64_tr_b16 v[82:83], v161 offset:768
	ds_read_b64_tr_b16 v[84:85], v146 offset:6144
	ds_read_b64_tr_b16 v[86:87], v161 offset:6912
	ds_read_b64_tr_b16 v[88:89], v146 offset:12288
	ds_read_b64_tr_b16 v[90:91], v161 offset:13056
	ds_read_b64_tr_b16 v[92:93], v146 offset:18432
	ds_read_b64_tr_b16 v[94:95], v161 offset:19200
	s_waitcnt lgkmcnt(6)
	v_mfma_f32_32x32x16_bf16 v[48:63], v[80:83], v[76:79], v[48:63]
	v_cvt_pk_bf16_f32 v66, v66, v67
	v_cvt_pk_bf16_f32 v67, v70, v71
	v_cvt_pk_bf16_f32 v71, v166, v167
	v_add_u32_e32 v166, s14, v153
	v_cvt_pk_bf16_f32 v69, v164, v165
	v_cvt_pk_bf16_f32 v70, v162, v163
	v_add_u32_e32 v167, s14, v154
	ds_read_b64_tr_b16 v[162:163], v166
	ds_read_b64_tr_b16 v[164:165], v167 offset:768
	ds_read_b64_tr_b16 v[176:177], v166 offset:6144
	ds_read_b64_tr_b16 v[178:179], v167 offset:6912
	ds_read_b64_tr_b16 v[204:205], v166 offset:12288
	ds_read_b64_tr_b16 v[206:207], v167 offset:13056
	ds_read_b64_tr_b16 v[208:209], v166 offset:18432
	ds_read_b64_tr_b16 v[210:211], v167 offset:19200
	s_waitcnt lgkmcnt(12)
	v_mfma_f32_32x32x16_bf16 v[48:63], v[84:87], v[72:75], v[48:63]
	s_add_i32 s14, s10, -2
	s_and_b32 s14, s14, 3
	s_mulk_i32 s14, 0x6000
	v_mov_b32_e32 v160, v159
	s_nop 1
	v_permlane32_swap_b32_e32 v159, v160
	s_waitcnt lgkmcnt(6)
	v_mfma_f32_32x32x16_bf16 v[32:47], v[162:165], v[76:79], v[32:47]
	v_mfma_f32_32x32x16_bf16 v[48:63], v[88:91], v[64:67], v[48:63]
	s_waitcnt lgkmcnt(4)
	v_mfma_f32_32x32x16_bf16 v[32:47], v[176:179], v[72:75], v[32:47]
	v_mfma_f32_32x32x16_bf16 v[48:63], v[92:95], v[68:71], v[48:63]
	ds_read_b64_tr_b16 v[80:81], v146 offset:128
	ds_read_b64_tr_b16 v[82:83], v161 offset:896
	ds_read_b64_tr_b16 v[92:93], v146 offset:6272
	ds_read_b64_tr_b16 v[94:95], v161 offset:7040
	ds_read_b64_tr_b16 v[212:213], v146 offset:12416
	ds_read_b64_tr_b16 v[214:215], v161 offset:13184
	ds_read_b64_tr_b16 v[88:89], v146 offset:18560
	ds_read_b64_tr_b16 v[90:91], v161 offset:19328
	v_add_u32_e32 v146, s14, v147
	v_add_u32_e32 v161, s14, v148
	s_waitcnt lgkmcnt(10)
	v_mfma_f32_32x32x16_bf16 v[32:47], v[204:207], v[64:67], v[32:47]
	ds_read_b64_tr_b16 v[84:85], v166 offset:128
	ds_read_b64_tr_b16 v[86:87], v167 offset:896
	ds_read_b64_tr_b16 v[162:163], v166 offset:6272
	ds_read_b64_tr_b16 v[164:165], v167 offset:7040
	ds_read_b64_tr_b16 v[176:177], v166 offset:12416
	ds_read_b64_tr_b16 v[178:179], v167 offset:13184
	ds_read_b64_tr_b16 v[204:205], v166 offset:18560
	ds_read_b64_tr_b16 v[206:207], v167 offset:19328
	v_add_u32_e32 v166, s14, v149
	v_add_u32_e32 v167, s14, v150
	s_waitcnt lgkmcnt(14)
	v_mfma_f32_32x32x16_bf16 v[0:15], v[80:83], v[76:79], v[0:15]
	s_waitcnt lgkmcnt(6)
	v_mfma_f32_32x32x16_bf16 v[16:31], v[84:87], v[76:79], v[16:31]
	v_mfma_f32_32x32x16_bf16 v[0:15], v[92:95], v[72:75], v[0:15]
	s_waitcnt lgkmcnt(4)
	v_mfma_f32_32x32x16_bf16 v[16:31], v[162:165], v[72:75], v[16:31]
	v_mfma_f32_32x32x16_bf16 v[0:15], v[212:215], v[64:67], v[0:15]
	s_waitcnt lgkmcnt(2)
	v_mfma_f32_32x32x16_bf16 v[16:31], v[176:179], v[64:67], v[16:31]
	v_mfma_f32_32x32x16_bf16 v[32:47], v[208:211], v[68:71], v[32:47]
	v_mfma_f32_32x32x16_bf16 v[0:15], v[88:91], v[68:71], v[0:15]
	s_waitcnt lgkmcnt(0)
	v_mfma_f32_32x32x16_bf16 v[16:31], v[204:207], v[68:71], v[16:31]
	ds_read_b128 v[64:67], v146
	ds_read_b128 v[68:71], v146 offset:12288
	ds_read_b128 v[162:165], v161
	ds_read_b128 v[176:179], v161 offset:12288
	ds_read_b128 v[204:207], v166
	ds_read_b128 v[208:211], v166 offset:12288
	ds_read_b128 v[212:215], v167
	ds_read_b128 v[216:219], v167 offset:12288
	s_waitcnt lgkmcnt(7)
	v_mfma_f32_32x32x16_bf16 v[80:95], v[64:67], v[112:115], 0
	s_waitcnt lgkmcnt(6)
	v_mfma_f32_32x32x16_bf16 v[64:79], v[68:71], v[112:115], 0
	s_waitcnt lgkmcnt(5)
	v_mfma_f32_32x32x16_bf16 v[80:95], v[162:165], v[116:119], v[80:95]
	ds_read_b128 v[162:165], v146 offset:128
	ds_read_b128 v[220:223], v146 offset:12416
	s_waitcnt lgkmcnt(6)
	v_mfma_f32_32x32x16_bf16 v[64:79], v[176:179], v[116:119], v[64:79]
	s_waitcnt lgkmcnt(5)
	v_mfma_f32_32x32x16_bf16 v[80:95], v[204:207], v[120:123], v[80:95]
	ds_read_b128 v[176:179], v161 offset:128
	ds_read_b128 v[204:207], v161 offset:12416
	s_waitcnt lgkmcnt(6)
	v_mfma_f32_32x32x16_bf16 v[64:79], v[208:211], v[120:123], v[64:79]
	s_waitcnt lgkmcnt(5)
	v_mfma_f32_32x32x16_bf16 v[80:95], v[212:215], v[124:127], v[80:95]
	ds_read_b128 v[208:211], v166 offset:128
	ds_read_b128 v[212:215], v166 offset:12416
	s_waitcnt lgkmcnt(6)
	v_mfma_f32_32x32x16_bf16 v[64:79], v[216:219], v[124:127], v[64:79]
	s_waitcnt lgkmcnt(5)
	v_mfma_f32_32x32x16_bf16 v[80:95], v[162:165], v[96:99], v[80:95]
	ds_read_b128 v[162:165], v167 offset:128
	ds_read_b128 v[216:219], v167 offset:12416
	s_waitcnt lgkmcnt(6)
	v_mfma_f32_32x32x16_bf16 v[64:79], v[220:223], v[96:99], v[64:79]
	s_waitcnt lgkmcnt(5)
	v_mfma_f32_32x32x16_bf16 v[80:95], v[176:179], v[100:103], v[80:95]
	ds_read_b128 v[176:179], v146 offset:256
	ds_read_b128 v[220:223], v146 offset:12544
	s_waitcnt lgkmcnt(6)
	v_mfma_f32_32x32x16_bf16 v[64:79], v[204:207], v[100:103], v[64:79]
	s_waitcnt lgkmcnt(5)
	v_mfma_f32_32x32x16_bf16 v[80:95], v[208:211], v[104:107], v[80:95]
	ds_read_b128 v[204:207], v161 offset:256
	ds_read_b128 v[208:211], v161 offset:12544
	s_waitcnt lgkmcnt(6)
	v_mfma_f32_32x32x16_bf16 v[64:79], v[212:215], v[104:107], v[64:79]
	s_waitcnt lgkmcnt(5)
	v_mfma_f32_32x32x16_bf16 v[80:95], v[162:165], v[108:111], v[80:95]
	ds_read_b128 v[162:165], v166 offset:256
	ds_read_b128 v[212:215], v166 offset:12544
	s_waitcnt lgkmcnt(6)
	v_mfma_f32_32x32x16_bf16 v[64:79], v[216:219], v[108:111], v[64:79]
	s_waitcnt lgkmcnt(5)
	v_mfma_f32_32x32x16_bf16 v[80:95], v[176:179], v[128:131], v[80:95]
	ds_read_b128 v[176:179], v167 offset:256
	ds_read_b128 v[216:219], v167 offset:12544
	s_waitcnt lgkmcnt(6)
	v_mfma_f32_32x32x16_bf16 v[64:79], v[220:223], v[128:131], v[64:79]
	s_waitcnt lgkmcnt(5)
	v_mfma_f32_32x32x16_bf16 v[80:95], v[204:207], v[132:135], v[80:95]
	s_waitcnt lgkmcnt(4)
	v_mfma_f32_32x32x16_bf16 v[64:79], v[208:211], v[132:135], v[64:79]
	s_waitcnt lgkmcnt(3)
	v_mfma_f32_32x32x16_bf16 v[80:95], v[162:165], v[136:139], v[80:95]
	s_waitcnt lgkmcnt(2)
	v_mfma_f32_32x32x16_bf16 v[64:79], v[212:215], v[136:139], v[64:79]
	s_waitcnt lgkmcnt(1)
	v_mfma_f32_32x32x16_bf16 v[80:95], v[176:179], v[140:143], v[80:95]
	s_waitcnt lgkmcnt(0)
	v_mfma_f32_32x32x16_bf16 v[64:79], v[216:219], v[140:143], v[64:79]
	s_cmp_le_u32 s7, s44
	s_cbranch_scc1 .LBB0_1248
	v_add_u32_e32 v146, 59, v156
	v_cmp_le_i32_e64 s[16:17], 0, v146
	v_cmp_le_i32_e64 s[18:19], 32, v146
	v_cmp_le_i32_e64 vcc, 1, v146
	s_nop 4
	v_cndmask_b32_e64 v80, v199, v80, s[16:17]
	v_cmp_le_i32_e64 s[16:17], 33, v146
	v_cndmask_b32_e64 v64, v199, v64, s[18:19]
	v_cmp_le_i32_e64 s[18:19], 2, v146
	v_cndmask_b32_e64 v81, v199, v81, vcc
	v_cmp_le_i32_e64 vcc, 34, v146
	v_cndmask_b32_e64 v65, v199, v65, s[16:17]
	v_cmp_le_i32_e64 s[16:17], 3, v146
	v_cndmask_b32_e64 v82, v199, v82, s[18:19]
	v_cmp_le_i32_e64 s[18:19], 35, v146
	v_cndmask_b32_e64 v66, v199, v66, vcc
	v_cmp_le_i32_e64 vcc, 8, v146
	v_cndmask_b32_e64 v83, v199, v83, s[16:17]
	v_cmp_le_i32_e64 s[16:17], 40, v146
	v_cndmask_b32_e64 v67, v199, v67, s[18:19]
	v_cmp_le_i32_e64 s[18:19], 9, v146
	v_cndmask_b32_e64 v84, v199, v84, vcc
	v_cmp_le_i32_e64 vcc, 41, v146
	v_cndmask_b32_e64 v68, v199, v68, s[16:17]
	v_cmp_le_i32_e64 s[16:17], 10, v146
	v_cndmask_b32_e64 v85, v199, v85, s[18:19]
	v_cmp_le_i32_e64 s[18:19], 42, v146
	v_cndmask_b32_e64 v69, v199, v69, vcc
	v_cmp_le_i32_e64 vcc, 11, v146
	v_cndmask_b32_e64 v86, v199, v86, s[16:17]
	v_cmp_le_i32_e64 s[16:17], 43, v146
	v_cndmask_b32_e64 v70, v199, v70, s[18:19]
	v_cmp_le_i32_e64 s[18:19], 16, v146
	v_cndmask_b32_e64 v87, v199, v87, vcc
	v_cmp_le_i32_e64 vcc, 48, v146
	v_cndmask_b32_e64 v71, v199, v71, s[16:17]
	v_cmp_le_i32_e64 s[16:17], 17, v146
	v_cndmask_b32_e64 v88, v199, v88, s[18:19]
	v_cmp_le_i32_e64 s[18:19], 49, v146
	v_cndmask_b32_e64 v72, v199, v72, vcc
	v_cmp_le_i32_e64 vcc, 18, v146
	v_cndmask_b32_e64 v89, v199, v89, s[16:17]
	v_cmp_le_i32_e64 s[16:17], 50, v146
	v_cndmask_b32_e64 v73, v199, v73, s[18:19]
	v_cmp_le_i32_e64 s[18:19], 19, v146
	v_cndmask_b32_e64 v90, v199, v90, vcc
	v_cmp_le_i32_e64 vcc, 51, v146
	v_cndmask_b32_e64 v74, v199, v74, s[16:17]
	v_cmp_le_i32_e64 s[16:17], 24, v146
	v_cndmask_b32_e64 v91, v199, v91, s[18:19]
	v_cmp_le_i32_e64 s[18:19], 56, v146
	v_cndmask_b32_e64 v75, v199, v75, vcc
	v_cmp_le_i32_e64 vcc, 25, v146
	v_cndmask_b32_e64 v92, v199, v92, s[16:17]
	v_cmp_le_i32_e64 s[16:17], 57, v146
	v_cndmask_b32_e64 v76, v199, v76, s[18:19]
	v_cmp_le_i32_e64 s[18:19], 26, v146
	v_cndmask_b32_e64 v93, v199, v93, vcc
	v_cmp_le_i32_e64 vcc, 58, v146
	v_cndmask_b32_e64 v77, v199, v77, s[16:17]
	v_cmp_le_i32_e64 s[16:17], 27, v146
	v_cndmask_b32_e64 v94, v199, v94, s[18:19]
	v_cmp_le_i32_e64 s[18:19], 59, v146
	v_cndmask_b32_e64 v78, v199, v78, vcc
	v_cndmask_b32_e64 v95, v199, v95, s[16:17]
	v_cndmask_b32_e64 v79, v199, v79, s[18:19]

.Lf_a:
	s_nop 7
	v_exp_f32_e32 v80, v80
	v_exp_f32_e32 v81, v81
	v_exp_f32_e32 v82, v82
	v_exp_f32_e32 v83, v83
	v_add_f32_e32 v146, 0, v80
	v_exp_f32_e32 v84, v84
	v_add_f32_e32 v146, v81, v146
	v_exp_f32_e32 v85, v85
	v_add_f32_e32 v146, v82, v146
	v_exp_f32_e32 v86, v86
	v_add_f32_e32 v146, v83, v146
	v_exp_f32_e32 v87, v87
	v_add_f32_e32 v146, v84, v146
	v_exp_f32_e32 v88, v88
	v_add_f32_e32 v146, v85, v146
	v_exp_f32_e32 v89, v89
	v_add_f32_e32 v146, v86, v146
	v_exp_f32_e32 v90, v90
	v_add_f32_e32 v146, v87, v146
	v_exp_f32_e32 v91, v91
	v_add_f32_e32 v146, v88, v146
	v_exp_f32_e32 v92, v92
	v_add_f32_e32 v146, v89, v146
	v_exp_f32_e32 v93, v93
	v_add_f32_e32 v146, v90, v146
	v_exp_f32_e32 v94, v94
	v_add_f32_e32 v146, v91, v146
	v_exp_f32_e32 v95, v95
	v_add_f32_e32 v146, v92, v146
	v_exp_f32_e32 v64, v64
	v_add_f32_e32 v146, v93, v146
	v_exp_f32_e32 v65, v65
	v_add_f32_e32 v146, v94, v146
	v_exp_f32_e32 v66, v66
	v_add_f32_e32 v146, v95, v146
	v_exp_f32_e32 v67, v67
	v_add_f32_e32 v146, v64, v146
	v_exp_f32_e32 v68, v68
	v_add_f32_e32 v146, v65, v146
	v_exp_f32_e32 v69, v69
	v_add_f32_e32 v146, v66, v146
	v_exp_f32_e32 v70, v70
	v_add_f32_e32 v146, v67, v146
	v_exp_f32_e32 v71, v71
	v_add_f32_e32 v146, v68, v146
	v_exp_f32_e32 v161, v72
	v_add_f32_e32 v146, v69, v146
	v_add_f32_e32 v146, v70, v146
	v_add_f32_e32 v146, v71, v146
	v_add_f32_e32 v72, v161, v146
	v_exp_f32_e32 v146, v73
	v_exp_f32_e32 v162, v74
	v_exp_f32_e32 v163, v75
	v_exp_f32_e32 v164, v76
	v_add_f32_e32 v72, v146, v72
	v_exp_f32_e32 v165, v77
	v_add_f32_e32 v72, v162, v72
	v_exp_f32_e32 v166, v78
	v_add_f32_e32 v72, v163, v72
	v_exp_f32_e32 v167, v79
	v_add_f32_e32 v72, v164, v72
	v_add_f32_e32 v72, v165, v72
	v_add_f32_e32 v72, v166, v72
	v_cvt_pk_bf16_f32 v76, v80, v81
	v_cvt_pk_bf16_f32 v77, v84, v85
	v_cvt_pk_bf16_f32 v78, v82, v83
	v_cvt_pk_bf16_f32 v79, v86, v87
	v_cvt_pk_bf16_f32 v64, v64, v65
	v_cvt_pk_bf16_f32 v65, v68, v69
	v_cvt_pk_bf16_f32 v68, v161, v146
	v_add_u32_e32 v146, s14, v151
	v_add_f32_e32 v159, v167, v72
	v_cvt_pk_bf16_f32 v72, v88, v89
	v_cvt_pk_bf16_f32 v73, v92, v93
	v_cvt_pk_bf16_f32 v74, v90, v91
	v_cvt_pk_bf16_f32 v75, v94, v95
	v_add_u32_e32 v161, s14, v152
	ds_read_b64_tr_b16 v[80:81], v146
	ds_read_b64_tr_b16 v[82:83], v161 offset:768
	ds_read_b64_tr_b16 v[84:85], v146 offset:6144
	ds_read_b64_tr_b16 v[86:87], v161 offset:6912
	ds_read_b64_tr_b16 v[88:89], v146 offset:12288
	ds_read_b64_tr_b16 v[90:91], v161 offset:13056
	ds_read_b64_tr_b16 v[92:93], v146 offset:18432
	ds_read_b64_tr_b16 v[94:95], v161 offset:19200
	s_waitcnt lgkmcnt(6)
	v_mfma_f32_32x32x16_bf16 v[48:63], v[80:83], v[76:79], v[48:63]
	v_cvt_pk_bf16_f32 v66, v66, v67
	v_cvt_pk_bf16_f32 v67, v70, v71
	v_cvt_pk_bf16_f32 v71, v166, v167
	v_add_u32_e32 v166, s14, v153
	v_cvt_pk_bf16_f32 v69, v164, v165
	v_cvt_pk_bf16_f32 v70, v162, v163
	v_add_u32_e32 v167, s14, v154
	ds_read_b64_tr_b16 v[162:163], v166
	ds_read_b64_tr_b16 v[164:165], v167 offset:768
	ds_read_b64_tr_b16 v[176:177], v166 offset:6144
	ds_read_b64_tr_b16 v[178:179], v167 offset:6912
	ds_read_b64_tr_b16 v[204:205], v166 offset:12288
	ds_read_b64_tr_b16 v[206:207], v167 offset:13056
	ds_read_b64_tr_b16 v[208:209], v166 offset:18432
	ds_read_b64_tr_b16 v[210:211], v167 offset:19200
	s_waitcnt lgkmcnt(12)
	v_mfma_f32_32x32x16_bf16 v[48:63], v[84:87], v[72:75], v[48:63]
	s_add_i32 s14, s10, -2
	s_and_b32 s14, s14, 3
	s_mulk_i32 s14, 0x6000
	s_waitcnt lgkmcnt(6)
	v_mfma_f32_32x32x16_bf16 v[32:47], v[162:165], v[76:79], v[32:47]
	v_mfma_f32_32x32x16_bf16 v[48:63], v[88:91], v[64:67], v[48:63]
	s_waitcnt lgkmcnt(4)
	v_mfma_f32_32x32x16_bf16 v[32:47], v[176:179], v[72:75], v[32:47]
	v_mfma_f32_32x32x16_bf16 v[48:63], v[92:95], v[68:71], v[48:63]
	ds_read_b64_tr_b16 v[80:81], v146 offset:128
	ds_read_b64_tr_b16 v[82:83], v161 offset:896
	ds_read_b64_tr_b16 v[92:93], v146 offset:6272
	ds_read_b64_tr_b16 v[94:95], v161 offset:7040
	ds_read_b64_tr_b16 v[212:213], v146 offset:12416
	ds_read_b64_tr_b16 v[214:215], v161 offset:13184
	ds_read_b64_tr_b16 v[88:89], v146 offset:18560
	ds_read_b64_tr_b16 v[90:91], v161 offset:19328
	v_add_u32_e32 v146, s14, v147
	v_add_u32_e32 v161, s14, v148
	s_waitcnt lgkmcnt(10)
	v_mfma_f32_32x32x16_bf16 v[32:47], v[204:207], v[64:67], v[32:47]
	ds_read_b64_tr_b16 v[84:85], v166 offset:128
	ds_read_b64_tr_b16 v[86:87], v167 offset:896
	ds_read_b64_tr_b16 v[162:163], v166 offset:6272
	ds_read_b64_tr_b16 v[164:165], v167 offset:7040
	ds_read_b64_tr_b16 v[176:177], v166 offset:12416
	ds_read_b64_tr_b16 v[178:179], v167 offset:13184
	ds_read_b64_tr_b16 v[204:205], v166 offset:18560
	ds_read_b64_tr_b16 v[206:207], v167 offset:19328
	v_add_u32_e32 v166, s14, v149
	v_add_u32_e32 v167, s14, v150
	s_waitcnt lgkmcnt(14)
	v_mfma_f32_32x32x16_bf16 v[0:15], v[80:83], v[76:79], v[0:15]
	s_waitcnt lgkmcnt(6)
	v_mfma_f32_32x32x16_bf16 v[16:31], v[84:87], v[76:79], v[16:31]
	v_mfma_f32_32x32x16_bf16 v[0:15], v[92:95], v[72:75], v[0:15]
	s_waitcnt lgkmcnt(4)
	v_mfma_f32_32x32x16_bf16 v[16:31], v[162:165], v[72:75], v[16:31]
	v_mfma_f32_32x32x16_bf16 v[0:15], v[212:215], v[64:67], v[0:15]
	s_waitcnt lgkmcnt(2)
	v_mfma_f32_32x32x16_bf16 v[16:31], v[176:179], v[64:67], v[16:31]
	v_mfma_f32_32x32x16_bf16 v[32:47], v[208:211], v[68:71], v[32:47]
	v_mfma_f32_32x32x16_bf16 v[0:15], v[88:91], v[68:71], v[0:15]
	s_waitcnt lgkmcnt(0)
	v_mfma_f32_32x32x16_bf16 v[16:31], v[204:207], v[68:71], v[16:31]
	ds_read_b128 v[64:67], v146
	ds_read_b128 v[68:71], v146 offset:12288
	ds_read_b128 v[162:165], v161
	ds_read_b128 v[176:179], v161 offset:12288
	ds_read_b128 v[204:207], v166
	ds_read_b128 v[208:211], v166 offset:12288
	ds_read_b128 v[212:215], v167
	ds_read_b128 v[216:219], v167 offset:12288
	s_waitcnt lgkmcnt(6)
	v_mfma_f32_32x32x16_bf16 v[80:95], v[64:67], v[112:115], 0
	v_mfma_f32_32x32x16_bf16 v[64:79], v[68:71], v[112:115], 0
	s_waitcnt lgkmcnt(4)
	v_mfma_f32_32x32x16_bf16 v[80:95], v[162:165], v[116:119], v[80:95]
	ds_read_b128 v[162:165], v146 offset:128
	ds_read_b128 v[220:223], v146 offset:12416
	v_mfma_f32_32x32x16_bf16 v[64:79], v[176:179], v[116:119], v[64:79]
	s_waitcnt lgkmcnt(4)
	v_mfma_f32_32x32x16_bf16 v[80:95], v[204:207], v[120:123], v[80:95]
	ds_read_b128 v[176:179], v161 offset:128
	ds_read_b128 v[204:207], v161 offset:12416
	v_mfma_f32_32x32x16_bf16 v[64:79], v[208:211], v[120:123], v[64:79]
	s_waitcnt lgkmcnt(4)
	v_mfma_f32_32x32x16_bf16 v[80:95], v[212:215], v[124:127], v[80:95]
	ds_read_b128 v[208:211], v166 offset:128
	ds_read_b128 v[212:215], v166 offset:12416
	v_mfma_f32_32x32x16_bf16 v[64:79], v[216:219], v[124:127], v[64:79]
	s_waitcnt lgkmcnt(4)
	v_mfma_f32_32x32x16_bf16 v[80:95], v[162:165], v[96:99], v[80:95]
	ds_read_b128 v[162:165], v167 offset:128
	ds_read_b128 v[216:219], v167 offset:12416
	v_mfma_f32_32x32x16_bf16 v[64:79], v[220:223], v[96:99], v[64:79]
	s_waitcnt lgkmcnt(4)
	v_mfma_f32_32x32x16_bf16 v[80:95], v[176:179], v[100:103], v[80:95]
	ds_read_b128 v[176:179], v146 offset:256
	ds_read_b128 v[220:223], v146 offset:12544
	v_mfma_f32_32x32x16_bf16 v[64:79], v[204:207], v[100:103], v[64:79]
	s_waitcnt lgkmcnt(4)
	v_mfma_f32_32x32x16_bf16 v[80:95], v[208:211], v[104:107], v[80:95]
	ds_read_b128 v[204:207], v161 offset:256
	ds_read_b128 v[208:211], v161 offset:12544
	v_mfma_f32_32x32x16_bf16 v[64:79], v[212:215], v[104:107], v[64:79]
	s_waitcnt lgkmcnt(4)
	v_mfma_f32_32x32x16_bf16 v[80:95], v[162:165], v[108:111], v[80:95]
	ds_read_b128 v[162:165], v166 offset:256
	ds_read_b128 v[212:215], v166 offset:12544
	v_mfma_f32_32x32x16_bf16 v[64:79], v[216:219], v[108:111], v[64:79]
	s_waitcnt lgkmcnt(4)
	v_mfma_f32_32x32x16_bf16 v[80:95], v[176:179], v[128:131], v[80:95]
	ds_read_b128 v[176:179], v167 offset:256
	ds_read_b128 v[216:219], v167 offset:12544
	v_mfma_f32_32x32x16_bf16 v[64:79], v[220:223], v[128:131], v[64:79]
	s_waitcnt lgkmcnt(4)
	v_mfma_f32_32x32x16_bf16 v[80:95], v[204:207], v[132:135], v[80:95]
	v_mfma_f32_32x32x16_bf16 v[64:79], v[208:211], v[132:135], v[64:79]
	s_waitcnt lgkmcnt(2)
	v_mfma_f32_32x32x16_bf16 v[80:95], v[162:165], v[136:139], v[80:95]
	v_mfma_f32_32x32x16_bf16 v[64:79], v[212:215], v[136:139], v[64:79]
	s_waitcnt lgkmcnt(0)
	v_mfma_f32_32x32x16_bf16 v[80:95], v[176:179], v[140:143], v[80:95]
	v_mfma_f32_32x32x16_bf16 v[64:79], v[216:219], v[140:143], v[64:79]
	s_cmp_le_u32 s7, s44
	s_cbranch_scc1 .Lf_b
	v_add_u32_e32 v146, 59, v156
	v_cmp_le_i32_e64 s[16:17], 0, v146
	v_cmp_le_i32_e64 s[18:19], 32, v146
	v_cmp_le_i32_e64 vcc, 1, v146
	s_nop 4
	v_cndmask_b32_e64 v80, v199, v80, s[16:17]
	v_cmp_le_i32_e64 s[16:17], 33, v146
	v_cndmask_b32_e64 v64, v199, v64, s[18:19]
	v_cmp_le_i32_e64 s[18:19], 2, v146
	v_cndmask_b32_e64 v81, v199, v81, vcc
	v_cmp_le_i32_e64 vcc, 34, v146
	v_cndmask_b32_e64 v65, v199, v65, s[16:17]
	v_cmp_le_i32_e64 s[16:17], 3, v146
	v_cndmask_b32_e64 v82, v199, v82, s[18:19]
	v_cmp_le_i32_e64 s[18:19], 35, v146
	v_cndmask_b32_e64 v66, v199, v66, vcc
	v_cmp_le_i32_e64 vcc, 8, v146
	v_cndmask_b32_e64 v83, v199, v83, s[16:17]
	v_cmp_le_i32_e64 s[16:17], 40, v146
	v_cndmask_b32_e64 v67, v199, v67, s[18:19]
	v_cmp_le_i32_e64 s[18:19], 9, v146
	v_cndmask_b32_e64 v84, v199, v84, vcc
	v_cmp_le_i32_e64 vcc, 41, v146
	v_cndmask_b32_e64 v68, v199, v68, s[16:17]
	v_cmp_le_i32_e64 s[16:17], 10, v146
	v_cndmask_b32_e64 v85, v199, v85, s[18:19]
	v_cmp_le_i32_e64 s[18:19], 42, v146
	v_cndmask_b32_e64 v69, v199, v69, vcc
	v_cmp_le_i32_e64 vcc, 11, v146
	v_cndmask_b32_e64 v86, v199, v86, s[16:17]
	v_cmp_le_i32_e64 s[16:17], 43, v146
	v_cndmask_b32_e64 v70, v199, v70, s[18:19]
	v_cmp_le_i32_e64 s[18:19], 16, v146
	v_cndmask_b32_e64 v87, v199, v87, vcc
	v_cmp_le_i32_e64 vcc, 48, v146
	v_cndmask_b32_e64 v71, v199, v71, s[16:17]
	v_cmp_le_i32_e64 s[16:17], 17, v146
	v_cndmask_b32_e64 v88, v199, v88, s[18:19]
	v_cmp_le_i32_e64 s[18:19], 49, v146
	v_cndmask_b32_e64 v72, v199, v72, vcc
	v_cmp_le_i32_e64 vcc, 18, v146
	v_cndmask_b32_e64 v89, v199, v89, s[16:17]
	v_cmp_le_i32_e64 s[16:17], 50, v146
	v_cndmask_b32_e64 v73, v199, v73, s[18:19]
	v_cmp_le_i32_e64 s[18:19], 19, v146
	v_cndmask_b32_e64 v90, v199, v90, vcc
	v_cmp_le_i32_e64 vcc, 51, v146
	v_cndmask_b32_e64 v74, v199, v74, s[16:17]
	v_cmp_le_i32_e64 s[16:17], 24, v146
	v_cndmask_b32_e64 v91, v199, v91, s[18:19]
	v_cmp_le_i32_e64 s[18:19], 56, v146
	v_cndmask_b32_e64 v75, v199, v75, vcc
	v_cmp_le_i32_e64 vcc, 25, v146
	v_cndmask_b32_e64 v92, v199, v92, s[16:17]
	v_cmp_le_i32_e64 s[16:17], 57, v146
	v_cndmask_b32_e64 v76, v199, v76, s[18:19]
	v_cmp_le_i32_e64 s[18:19], 26, v146
	v_cndmask_b32_e64 v93, v199, v93, vcc
	v_cmp_le_i32_e64 vcc, 58, v146
	v_cndmask_b32_e64 v77, v199, v77, s[16:17]
	v_cmp_le_i32_e64 s[16:17], 27, v146
	v_cndmask_b32_e64 v94, v199, v94, s[18:19]
	v_cmp_le_i32_e64 s[18:19], 59, v146
	v_cndmask_b32_e64 v78, v199, v78, vcc
	v_cndmask_b32_e64 v95, v199, v95, s[16:17]
	v_cndmask_b32_e64 v79, v199, v79, s[18:19]
.Lf_b:
	s_nop 9
	v_exp_f32_e32 v170, v64
	v_exp_f32_e32 v171, v65
	v_exp_f32_e32 v176, v66
	v_exp_f32_e32 v177, v67
	v_exp_f32_e32 v178, v68
	v_exp_f32_e32 v179, v69
	v_exp_f32_e32 v161, v80
	v_exp_f32_e32 v185, v70
	v_exp_f32_e32 v162, v81
	v_exp_f32_e32 v187, v71
	v_exp_f32_e32 v163, v82
	v_exp_f32_e32 v203, v72
	v_exp_f32_e32 v164, v83
	v_exp_f32_e32 v204, v73
	v_exp_f32_e32 v165, v84
	v_exp_f32_e32 v205, v74
	v_exp_f32_e32 v166, v85
	v_exp_f32_e32 v206, v75
	v_exp_f32_e32 v167, v86
	v_exp_f32_e32 v207, v76
	v_add_u32_e32 v209, s14, v151
	v_exp_f32_e32 v168, v87
	v_exp_f32_e32 v208, v77
	v_add_u32_e32 v210, s14, v152
	ds_read_b64_tr_b16 v[64:65], v209
	ds_read_b64_tr_b16 v[66:67], v210 offset:768
	v_exp_f32_e32 v88, v88
	v_exp_f32_e32 v89, v89
	v_exp_f32_e32 v90, v90
	v_exp_f32_e32 v91, v91
	v_cvt_pk_bf16_f32 v72, v161, v162
	v_cvt_pk_bf16_f32 v73, v165, v166
	v_cvt_pk_bf16_f32 v74, v163, v164
	v_cvt_pk_bf16_f32 v75, v167, v168
	v_exp_f32_e32 v92, v92
	s_waitcnt lgkmcnt(0)
	v_mfma_f32_32x32x16_bf16 v[48:63], v[64:67], v[72:75], v[48:63]
	v_exp_f32_e32 v93, v93
	v_exp_f32_e32 v94, v94
	v_exp_f32_e32 v95, v95
	v_exp_f32_e32 v211, v78
	ds_read_b64_tr_b16 v[68:69], v209 offset:6144
	ds_read_b64_tr_b16 v[70:71], v210 offset:6912
	v_mov_b32_e32 v80, v79
	v_cvt_pk_bf16_f32 v76, v88, v89
	v_cvt_pk_bf16_f32 v77, v92, v93
	v_cvt_pk_bf16_f32 v78, v90, v91
	v_cvt_pk_bf16_f32 v79, v94, v95
	ds_read_b64_tr_b16 v[64:65], v209 offset:12288
	ds_read_b64_tr_b16 v[66:67], v210 offset:13056
	s_waitcnt lgkmcnt(2)
	v_mfma_f32_32x32x16_bf16 v[48:63], v[68:71], v[76:79], v[48:63]
	v_cvt_pk_bf16_f32 v68, v170, v171
	v_cvt_pk_bf16_f32 v69, v178, v179
	v_cvt_pk_bf16_f32 v70, v176, v177
	v_cvt_pk_bf16_f32 v71, v185, v187
	v_add_u32_e32 v213, s14, v153
	v_exp_f32_e32 v212, v80
	ds_read_b64_tr_b16 v[80:81], v209 offset:18432
	ds_read_b64_tr_b16 v[82:83], v210 offset:19200
	s_waitcnt lgkmcnt(2)
	v_mfma_f32_32x32x16_bf16 v[48:63], v[64:67], v[68:71], v[48:63]
	ds_read_b64_tr_b16 v[84:85], v213
	v_cvt_pk_bf16_f32 v64, v203, v204
	v_cvt_pk_bf16_f32 v65, v207, v208
	v_cvt_pk_bf16_f32 v66, v205, v206
	v_cvt_pk_bf16_f32 v67, v211, v212
	v_add_u32_e32 v214, s14, v154
	s_waitcnt lgkmcnt(1)
	v_mfma_f32_32x32x16_bf16 v[48:63], v[80:83], v[64:67], v[48:63]
	ds_read_b64_tr_b16 v[86:87], v214 offset:768
	ds_read_b64_tr_b16 v[80:81], v213 offset:6144
	v_add_f32_e32 v158, v158, v159
	s_addk_i32 s12, 0x1000
	s_add_i32 s11, s11, 4
	s_add_i32 s10, s10, 2
	s_addk_i32 s7, 0x80
	v_add_u32_e32 v155, 32, v155
	s_waitcnt lgkmcnt(1)
	v_mfma_f32_32x32x16_bf16 v[32:47], v[84:87], v[72:75], v[32:47]
	ds_read_b64_tr_b16 v[82:83], v214 offset:6912
	ds_read_b64_tr_b16 v[84:85], v213 offset:12288
	s_cmp_ge_u32 s13, s9
	v_add_u32_e32 v156, 0xffffff80, v156
	s_waitcnt lgkmcnt(1)
	v_mfma_f32_32x32x16_bf16 v[32:47], v[80:83], v[76:79], v[32:47]
	ds_read_b64_tr_b16 v[86:87], v214 offset:13056
	ds_read_b64_tr_b16 v[80:81], v213 offset:18432
	s_waitcnt lgkmcnt(1)
	v_mfma_f32_32x32x16_bf16 v[32:47], v[84:87], v[68:71], v[32:47]
	ds_read_b64_tr_b16 v[82:83], v214 offset:19200
	ds_read_b64_tr_b16 v[84:85], v209 offset:128
	ds_read_b64_tr_b16 v[86:87], v210 offset:896
	s_waitcnt lgkmcnt(0)
	v_mfma_f32_32x32x16_bf16 v[0:15], v[84:87], v[72:75], v[0:15]
	v_add_f32_e32 v84, 0, v161
	v_add_f32_e32 v84, v162, v84
	v_add_f32_e32 v84, v163, v84
	v_add_f32_e32 v84, v164, v84
	v_add_f32_e32 v144, v165, v84
	v_mfma_f32_32x32x16_bf16 v[32:47], v[80:83], v[64:67], v[32:47]
	ds_read_b64_tr_b16 v[80:81], v209 offset:6272
	ds_read_b64_tr_b16 v[82:83], v210 offset:7040
	ds_read_b64_tr_b16 v[84:85], v209 offset:12416
	ds_read_b64_tr_b16 v[86:87], v210 offset:13184
	s_waitcnt lgkmcnt(2)
	v_mfma_f32_32x32x16_bf16 v[0:15], v[80:83], v[76:79], v[0:15]
	v_add_f32_e32 v80, v166, v144
	v_add_f32_e32 v80, v167, v80
	v_add_f32_e32 v80, v168, v80
	v_add_f32_e32 v80, v88, v80
	v_add_f32_e32 v88, v89, v80
	ds_read_b64_tr_b16 v[80:81], v209 offset:18560
	ds_read_b64_tr_b16 v[82:83], v210 offset:19328
	s_waitcnt lgkmcnt(2)
	v_mfma_f32_32x32x16_bf16 v[0:15], v[84:87], v[68:71], v[0:15]
	v_add_f32_e32 v84, v90, v88
	v_add_f32_e32 v84, v91, v84
	v_add_f32_e32 v84, v92, v84
	v_add_f32_e32 v84, v93, v84
	v_add_f32_e32 v88, v94, v84
	ds_read_b64_tr_b16 v[84:85], v213 offset:128
	ds_read_b64_tr_b16 v[86:87], v214 offset:896
	s_waitcnt lgkmcnt(2)
	v_mfma_f32_32x32x16_bf16 v[0:15], v[80:83], v[64:67], v[0:15]
	v_add_f32_e32 v80, v95, v88
	v_add_f32_e32 v80, v170, v80
	v_add_f32_e32 v80, v171, v80
	v_add_f32_e32 v80, v176, v80
	v_add_f32_e32 v88, v177, v80
	ds_read_b64_tr_b16 v[80:81], v213 offset:6272
	ds_read_b64_tr_b16 v[82:83], v214 offset:7040
	s_waitcnt lgkmcnt(2)
	v_mfma_f32_32x32x16_bf16 v[16:31], v[84:87], v[72:75], v[16:31]
	v_add_f32_e32 v72, v178, v88
	v_add_f32_e32 v72, v179, v72
	v_add_f32_e32 v72, v185, v72
	v_add_f32_e32 v72, v187, v72
	v_add_f32_e32 v84, v203, v72
	ds_read_b64_tr_b16 v[72:73], v213 offset:12416
	ds_read_b64_tr_b16 v[74:75], v214 offset:13184
	s_waitcnt lgkmcnt(2)
	v_mfma_f32_32x32x16_bf16 v[16:31], v[80:83], v[76:79], v[16:31]
	v_add_f32_e32 v76, v204, v84
	v_add_f32_e32 v76, v205, v76
	v_add_f32_e32 v76, v206, v76
	v_add_f32_e32 v76, v207, v76
	v_add_f32_e32 v80, v208, v76
	ds_read_b64_tr_b16 v[76:77], v213 offset:18560
	ds_read_b64_tr_b16 v[78:79], v214 offset:19328
	s_waitcnt vmcnt(0)
	s_waitcnt lgkmcnt(2)
	v_mfma_f32_32x32x16_bf16 v[16:31], v[72:75], v[68:71], v[16:31]
	v_add_f32_e32 v68, v211, v80
	v_add_f32_e32 v68, v212, v68
	v_add_f32_e32 v158, v158, v68
	s_waitcnt lgkmcnt(0)
	v_mfma_f32_32x32x16_bf16 v[16:31], v[76:79], v[64:67], v[16:31]
	s_barrier
	s_cbranch_scc1 .LBB0_1250
	s_branch .LBB0_1238
.LBB0_1250:
	s_cmp_eq_u32 s101, 0
	s_cbranch_scc1 .Lg_done
	v_mov_b32_e32 v160, v158
	s_nop 1
	v_permlane32_swap_b32_e32 v158, v160
	v_add_f32_e32 v158, v158, v160
	v_cmp_gt_f32_e32 vcc, 0x7149f2ca, v158
	s_mov_b64 s[16:17], vcc
	v_cmp_lt_f32_e32 vcc, 0x0da24260, v158
	s_and_b64 vcc, vcc, s[16:17]
	v_mov_b32_e32 v159, 0x20180
	s_cmp_eq_u64 vcc, exec
	s_cbranch_scc1 .Lg_vote
	v_mov_b32_e32 v160, 1
	ds_write_b32 v159, v160
